# v24 + mini-GEMM prefetch 4 K-chunks deep + final phase: tok_rank pair loaded as one dwordx2 together with tok_e (two dependent round trips per row removed)
# baseline (speedup 1.0000x reference)
; #define SEAM(k) do { if (IN(k) && IN((k) + 1)) { if ((MK_TAIL_MASK >> (k)) & 1u) moe_pull(F, (k), 0); if ((k) == 9) moe_pull(F, -1, NQ_LATE); if ((k) == 15) moe_pull(F, -1, NQ); xcd_barrier(bar); { int t_ = threadIdx.x; asm volatile("" : "+v"(t_)); F.tid = t_; F.lane = t_ & 63; } } } while (0)
; __global__ void __launch_bounds__(NWAVES * 64, 2) fwd_kernel(Args args) {
;     ...
;     if (IN(5)) { pg8::Gemm g{WSP(const pg8::bf16_t, WS_AO), WSP(const pg8::bf16_t, WS_WOUT0), MT, DM, DM, 0, DM, 0, 0}; pg8::StaticOrder S; S.init(MT, DM, F.G, (int)blockIdx.x);
;         pg8::EpiResH<false> E{F.in[0], F.in[2], WSP(pg8::bf16_t, WS_H), WSP(const float, WS_MOD0) + 2 * DM, 1.0f};
;         pg8::gemm_phase<pg8::EpiResH<false>, pg8::StaticOrder, true, true>(F.lds, g, S, E); } SEAM(5);
.LBB0_546:
	v_readlane_b32 s98, v250, 62
	v_and_b32_e32 v2, 15, v0
	v_bfe_u32 v3, v0, 4, 2
	v_lshrrev_b32_e32 v4, 6, v0
	v_lshrrev_b32_e32 v5, 1, v4
	v_and_b32_e32 v6, 1, v4
	s_lshr_b32 s99, s98, 5
	s_lshl_b32 s99, s99, 6
	s_and_b32 s100, s98, 31
	s_lshl_b32 s100, s100, 6
	v_lshl_add_u32 v7, v5, 4, v2
	v_add_u32_e32 v7, s99, v7
	v_lshrrev_b32_e32 v8, 4, v0
	v_lshlrev_b32_e32 v9, 4, v2
	v_add_u32_e32 v10, s99, v8
	v_mul_u32_u24_e32 v10, 0x1000, v10
	v_add_u32_e32 v10, v10, v9
	s_mov_b32 s101, 0x25c00000
	v_add_u32_e32 v10, s101, v10
	v_mov_b32_e32 v11, 0
	v_add_u32_e32 v12, 0x20000, v10
	v_mov_b32_e32 v13, 0
	v_add_u32_e32 v14, s100, v8
	v_mul_u32_u24_e32 v14, 0x1000, v14
	v_add_u32_e32 v14, v14, v9
	s_mov_b32 s101, 0x2600000
	v_add_u32_e32 v14, s101, v14
	v_mov_b32_e32 v15, 0
	v_add_u32_e32 v16, 0x20000, v14
	v_mov_b32_e32 v17, 0
	v_lshl_add_u64 v[10:11], s[88:89], 0, v[10:11]
	v_lshl_add_u64 v[12:13], s[88:89], 0, v[12:13]
	v_lshl_add_u64 v[14:15], s[88:89], 0, v[14:15]
	v_lshl_add_u64 v[16:17], s[88:89], 0, v[16:17]
	v_mul_u32_u24_e32 v18, 272, v8
	v_add_u32_e32 v18, v18, v9
	v_lshl_add_u32 v19, v5, 4, v2
	v_mul_u32_u24_e32 v19, 272, v19
	v_lshl_add_u32 v19, v3, 4, v19
	v_lshl_add_u32 v28, v6, 5, v2
	v_mul_u32_u24_e32 v28, 272, v28
	v_lshl_add_u32 v28, v3, 4, v28
	v_add_u32_e32 v28, 17408, v28
	v_mov_b32_e32 v112, 0x400
	v_mov_b32_e32 v113, 0
	v_lshl_add_u32 v116, v6, 5, s100
	v_lshl_add_u32 v116, v3, 2, v116
	v_lshlrev_b32_e32 v118, 2, v116
	v_lshl_add_u32 v128, v7, 13, v118
	v_mov_b32_e32 v129, 0
	v_readlane_b32 s100, v250, 12
	v_readlane_b32 s101, v250, 13
	s_nop 4
	v_lshl_add_u64 v[128:129], s[100:101], 0, v[128:129]
	s_mov_b32 s101, 0x11c000
	v_add_u32_e32 v130, s101, v118
	v_mov_b32_e32 v131, 0
	v_lshl_add_u64 v[130:131], s[88:89], 0, v[130:131]
	global_load_dwordx4 v[132:135], v[128:129], off
	global_load_dwordx4 v[136:139], v[128:129], off offset:64
	global_load_dwordx4 v[140:143], v[130:131], off
	global_load_dwordx4 v[144:147], v[130:131], off offset:64
	v_mov_b32_e32 v20, 0
	v_mov_b32_e32 v21, 0
	v_mov_b32_e32 v22, 0
	v_mov_b32_e32 v23, 0
	v_mov_b32_e32 v24, 0
	v_mov_b32_e32 v25, 0
	v_mov_b32_e32 v26, 0
	v_mov_b32_e32 v27, 0
	global_load_dwordx4 v[32:35], v[10:11], off offset:0
	global_load_dwordx4 v[36:39], v[12:13], off offset:0
	global_load_dwordx4 v[40:43], v[14:15], off offset:0
	global_load_dwordx4 v[44:47], v[16:17], off offset:0
	global_load_dwordx4 v[48:51], v[10:11], off offset:256
	global_load_dwordx4 v[52:55], v[12:13], off offset:256
	global_load_dwordx4 v[56:59], v[14:15], off offset:256
	global_load_dwordx4 v[60:63], v[16:17], off offset:256
	global_load_dwordx4 v[160:163], v[10:11], off offset:512
	global_load_dwordx4 v[164:167], v[12:13], off offset:512
	global_load_dwordx4 v[168:171], v[14:15], off offset:512
	global_load_dwordx4 v[172:175], v[16:17], off offset:512
	global_load_dwordx4 v[176:179], v[10:11], off offset:768
	global_load_dwordx4 v[180:183], v[12:13], off offset:768
	global_load_dwordx4 v[184:187], v[14:15], off offset:768
	global_load_dwordx4 v[188:191], v[16:17], off offset:768
	s_waitcnt vmcnt(12)
	ds_write_b128 v18, v[32:35] offset:0
	ds_write_b128 v18, v[36:39] offset:8704
	ds_write_b128 v18, v[40:43] offset:17408
	ds_write_b128 v18, v[44:47] offset:26112
	s_waitcnt lgkmcnt(0)
	s_barrier
	s_mov_b32 s101, 4
.Lmg5_kloop:
	global_load_dwordx4 v[32:35], v[10:11], off offset:1024
	global_load_dwordx4 v[36:39], v[12:13], off offset:1024
	global_load_dwordx4 v[40:43], v[14:15], off offset:1024
	global_load_dwordx4 v[44:47], v[16:17], off offset:1024
	s_waitcnt vmcnt(12)
	ds_write_b128 v18, v[48:51] offset:34816
	ds_write_b128 v18, v[52:55] offset:43520
	ds_write_b128 v18, v[56:59] offset:52224
	ds_write_b128 v18, v[60:63] offset:60928
	ds_read_b128 v[64:67], v19 offset:0
	ds_read_b128 v[68:71], v19 offset:64
	ds_read_b128 v[72:75], v19 offset:128
	ds_read_b128 v[76:79], v19 offset:192
	ds_read_b128 v[80:83], v28 offset:0
	ds_read_b128 v[84:87], v28 offset:64
	ds_read_b128 v[88:91], v28 offset:128
	ds_read_b128 v[92:95], v28 offset:192
	ds_read_b128 v[96:99], v28 offset:4352
	ds_read_b128 v[100:103], v28 offset:4416
	ds_read_b128 v[104:107], v28 offset:4480
	ds_read_b128 v[108:111], v28 offset:4544
	s_waitcnt lgkmcnt(0)
	v_mfma_f32_16x16x32_bf16 v[20:23], v[80:83], v[64:67], v[20:23]
	v_mfma_f32_16x16x32_bf16 v[24:27], v[96:99], v[64:67], v[24:27]
	v_mfma_f32_16x16x32_bf16 v[20:23], v[84:87], v[68:71], v[20:23]
	v_mfma_f32_16x16x32_bf16 v[24:27], v[100:103], v[68:71], v[24:27]
	v_mfma_f32_16x16x32_bf16 v[20:23], v[88:91], v[72:75], v[20:23]
	v_mfma_f32_16x16x32_bf16 v[24:27], v[104:107], v[72:75], v[24:27]
	v_mfma_f32_16x16x32_bf16 v[20:23], v[92:95], v[76:79], v[20:23]
	v_mfma_f32_16x16x32_bf16 v[24:27], v[108:111], v[76:79], v[24:27]
	s_waitcnt lgkmcnt(0)
	s_barrier
	global_load_dwordx4 v[48:51], v[10:11], off offset:1280
	global_load_dwordx4 v[52:55], v[12:13], off offset:1280
	global_load_dwordx4 v[56:59], v[14:15], off offset:1280
	global_load_dwordx4 v[60:63], v[16:17], off offset:1280
	s_waitcnt vmcnt(12)
	ds_write_b128 v18, v[160:163] offset:0
	ds_write_b128 v18, v[164:167] offset:8704
	ds_write_b128 v18, v[168:171] offset:17408
	ds_write_b128 v18, v[172:175] offset:26112
	ds_read_b128 v[64:67], v19 offset:34816
	ds_read_b128 v[68:71], v19 offset:34880
	ds_read_b128 v[72:75], v19 offset:34944
	ds_read_b128 v[76:79], v19 offset:35008
	ds_read_b128 v[80:83], v28 offset:34816
	ds_read_b128 v[84:87], v28 offset:34880
	ds_read_b128 v[88:91], v28 offset:34944
	ds_read_b128 v[92:95], v28 offset:35008
	ds_read_b128 v[96:99], v28 offset:39168
	ds_read_b128 v[100:103], v28 offset:39232
	ds_read_b128 v[104:107], v28 offset:39296
	ds_read_b128 v[108:111], v28 offset:39360
	s_waitcnt lgkmcnt(0)
	v_mfma_f32_16x16x32_bf16 v[20:23], v[80:83], v[64:67], v[20:23]
	v_mfma_f32_16x16x32_bf16 v[24:27], v[96:99], v[64:67], v[24:27]
	v_mfma_f32_16x16x32_bf16 v[20:23], v[84:87], v[68:71], v[20:23]
	v_mfma_f32_16x16x32_bf16 v[24:27], v[100:103], v[68:71], v[24:27]
	v_mfma_f32_16x16x32_bf16 v[20:23], v[88:91], v[72:75], v[20:23]
	v_mfma_f32_16x16x32_bf16 v[24:27], v[104:107], v[72:75], v[24:27]
	v_mfma_f32_16x16x32_bf16 v[20:23], v[92:95], v[76:79], v[20:23]
	v_mfma_f32_16x16x32_bf16 v[24:27], v[108:111], v[76:79], v[24:27]
	s_waitcnt lgkmcnt(0)
	s_barrier
; __device__ __forceinline__ unsigned cvt_pk_bf16(float lo, float hi) { unsigned r; asm volatile("v_cvt_pk_bf16_f32 %0, %1, %2" : "=v"(r) : "v"(lo), "v"(hi)); return r; }
;     __device__ __forceinline__ void operator()(const f32x4 (&acc)[2][2][4][2], const Unit& u, int wr, int wc, int fr, int fq) const {
;     ...
;                     for (int bj = 0; bj < 2; ++bj) { const f32x4 r0 = bs[m][bj][0] + gg[bj][0] * acc[ai][bj][m][0], r1 = bs[m][bj][1] + gg[bj][1] * acc[ai][bj][m][1];
;                         u32x4 w; w.x = cvt_pk_bf16(r0[0], r0[1]); w.y = cvt_pk_bf16(r0[2], r0[3]); w.z = cvt_pk_bf16(r1[0], r1[1]); w.w = cvt_pk_bf16(r1[2], r1[3]);
;                         *(u32x4*)(H + (size_t)(row0 + ai * HALF + m * 16) * 2048 + col0 + bj * HALF) = w; }
; __device__ __forceinline__ void xcd_barrier(const XcdBarrier& b) {
;     asm volatile("s_waitcnt vmcnt(0)" ::: "memory");
;     __syncthreads();
;     if (threadIdx.x == 0) {
;         unsigned* bar = b.bar;
;         __builtin_amdgcn_s_waitcnt(0);
;         unsigned nloc = b.st[0], nx = b.st[1];
;         if (nloc == 0u) { xcd_barrier_complete(bar, b.x, b.total, nloc, nx); b.st[0] = nloc; b.st[1] = nx; }
	global_load_dwordx4 v[160:163], v[10:11], off offset:1536
	global_load_dwordx4 v[164:167], v[12:13], off offset:1536
	global_load_dwordx4 v[168:171], v[14:15], off offset:1536
	global_load_dwordx4 v[172:175], v[16:17], off offset:1536
	s_waitcnt vmcnt(12)
	ds_write_b128 v18, v[176:179] offset:34816
	ds_write_b128 v18, v[180:183] offset:43520
	ds_write_b128 v18, v[184:187] offset:52224
	ds_write_b128 v18, v[188:191] offset:60928
	ds_read_b128 v[64:67], v19 offset:0
	ds_read_b128 v[68:71], v19 offset:64
	ds_read_b128 v[72:75], v19 offset:128
	ds_read_b128 v[76:79], v19 offset:192
	ds_read_b128 v[80:83], v28 offset:0
	ds_read_b128 v[84:87], v28 offset:64
	ds_read_b128 v[88:91], v28 offset:128
	ds_read_b128 v[92:95], v28 offset:192
	ds_read_b128 v[96:99], v28 offset:4352
	ds_read_b128 v[100:103], v28 offset:4416
	ds_read_b128 v[104:107], v28 offset:4480
	ds_read_b128 v[108:111], v28 offset:4544
	s_waitcnt lgkmcnt(0)
	v_mfma_f32_16x16x32_bf16 v[20:23], v[80:83], v[64:67], v[20:23]
	v_mfma_f32_16x16x32_bf16 v[24:27], v[96:99], v[64:67], v[24:27]
	v_mfma_f32_16x16x32_bf16 v[20:23], v[84:87], v[68:71], v[20:23]
	v_mfma_f32_16x16x32_bf16 v[24:27], v[100:103], v[68:71], v[24:27]
	v_mfma_f32_16x16x32_bf16 v[20:23], v[88:91], v[72:75], v[20:23]
	v_mfma_f32_16x16x32_bf16 v[24:27], v[104:107], v[72:75], v[24:27]
	v_mfma_f32_16x16x32_bf16 v[20:23], v[92:95], v[76:79], v[20:23]
	v_mfma_f32_16x16x32_bf16 v[24:27], v[108:111], v[76:79], v[24:27]
	s_waitcnt lgkmcnt(0)
	s_barrier
	global_load_dwordx4 v[176:179], v[10:11], off offset:1792
	global_load_dwordx4 v[180:183], v[12:13], off offset:1792
	global_load_dwordx4 v[184:187], v[14:15], off offset:1792
	global_load_dwordx4 v[188:191], v[16:17], off offset:1792
	s_waitcnt vmcnt(12)
	ds_write_b128 v18, v[32:35] offset:0
	ds_write_b128 v18, v[36:39] offset:8704
	ds_write_b128 v18, v[40:43] offset:17408
	ds_write_b128 v18, v[44:47] offset:26112
	ds_read_b128 v[64:67], v19 offset:34816
	ds_read_b128 v[68:71], v19 offset:34880
	ds_read_b128 v[72:75], v19 offset:34944
	ds_read_b128 v[76:79], v19 offset:35008
	ds_read_b128 v[80:83], v28 offset:34816
	ds_read_b128 v[84:87], v28 offset:34880
	ds_read_b128 v[88:91], v28 offset:34944
	ds_read_b128 v[92:95], v28 offset:35008
	ds_read_b128 v[96:99], v28 offset:39168
	ds_read_b128 v[100:103], v28 offset:39232
	ds_read_b128 v[104:107], v28 offset:39296
	ds_read_b128 v[108:111], v28 offset:39360
	s_waitcnt lgkmcnt(0)
	v_mfma_f32_16x16x32_bf16 v[20:23], v[80:83], v[64:67], v[20:23]
	v_mfma_f32_16x16x32_bf16 v[24:27], v[96:99], v[64:67], v[24:27]
	v_mfma_f32_16x16x32_bf16 v[20:23], v[84:87], v[68:71], v[20:23]
	v_mfma_f32_16x16x32_bf16 v[24:27], v[100:103], v[68:71], v[24:27]
	v_mfma_f32_16x16x32_bf16 v[20:23], v[88:91], v[72:75], v[20:23]
	v_mfma_f32_16x16x32_bf16 v[24:27], v[104:107], v[72:75], v[24:27]
	v_mfma_f32_16x16x32_bf16 v[20:23], v[92:95], v[76:79], v[20:23]
	v_mfma_f32_16x16x32_bf16 v[24:27], v[108:111], v[76:79], v[24:27]
	v_lshl_add_u64 v[10:11], v[10:11], 0, v[112:113]
	v_lshl_add_u64 v[12:13], v[12:13], 0, v[112:113]
	v_lshl_add_u64 v[14:15], v[14:15], 0, v[112:113]
	v_lshl_add_u64 v[16:17], v[16:17], 0, v[112:113]
	s_waitcnt lgkmcnt(0)
	s_barrier
	s_sub_u32 s101, s101, 1
	s_cmp_lg_u32 s101, 0
	s_cbranch_scc1 .Lmg5_kloop
	s_nop 7
	s_nop 7
	v_lshlrev_b32_e32 v116, 1, v116
	v_lshl_add_u32 v116, v7, 12, v116
	s_mov_b32 s101, 0x51800000
	v_add_u32_e32 v116, s101, v116
	v_mov_b32_e32 v117, 0
	v_lshl_add_u64 v[116:117], s[88:89], 0, v[116:117]
	v_fma_f32 v20, v140, v20, v132
	v_fma_f32 v21, v141, v21, v133
	v_fma_f32 v22, v142, v22, v134
	v_fma_f32 v23, v143, v23, v135
	v_fma_f32 v24, v144, v24, v136
	v_fma_f32 v25, v145, v25, v137
	v_fma_f32 v26, v146, v26, v138
	v_fma_f32 v27, v147, v27, v139
	v_cvt_pk_bf16_f32 v28, v20, v21
	v_cvt_pk_bf16_f32 v29, v22, v23
	v_cvt_pk_bf16_f32 v30, v24, v25
	v_cvt_pk_bf16_f32 v31, v26, v27
	global_store_dwordx2 v[116:117], v[28:29], off
	global_store_dwordx2 v[116:117], v[30:31], off offset:32
	s_cmp_gt_i32 s91, 6
	s_cselect_b64 s[0:1], -1, 0
	s_and_b64 s[2:3], s[2:3], s[0:1]
	s_andn2_b64 vcc, exec, s[2:3]
	s_cbranch_vccnz .LBB0_600
	s_waitcnt vmcnt(0)
	s_waitcnt vmcnt(0) lgkmcnt(0)
	s_barrier
	s_mov_b64 s[2:3], exec
	v_readlane_b32 s4, v250, 59
	v_readlane_b32 s5, v250, 60
	s_and_b64 s[4:5], s[2:3], s[4:5]
	s_mov_b64 exec, s[4:5]
	s_cbranch_execz .LBB0_599
	s_add_i32 s4, 0, 0x25020
	v_mov_b32_e32 v1, s4
	s_waitcnt vmcnt(0) expcnt(0) lgkmcnt(0)
	ds_read_b32 v3, v1
	s_add_i32 s4, 0, 0x25024
	v_mov_b32_e32 v1, s4
	ds_read_b32 v1, v1
	s_waitcnt lgkmcnt(1)
	v_cmp_ne_u32_e32 vcc, 0, v3
	s_cbranch_vccnz .LBB0_563
	s_add_u32 s4, s88, 0x4200
	s_addc_u32 s5, s89, 0
	s_add_u32 s6, s88, 0x4400
	s_addc_u32 s7, s89, 0
	s_add_u32 s8, s88, 0x4500
	s_addc_u32 s9, s89, 0
	s_add_u32 s10, s88, 0x4600
	s_addc_u32 s11, s89, 0
	s_add_u32 s12, s88, 0x4700
	s_addc_u32 s13, s89, 0
	s_add_u32 s14, s88, 0x4800
	s_addc_u32 s15, s89, 0
	s_add_u32 s16, s88, 0x4900
	s_addc_u32 s17, s89, 0
	s_add_u32 s18, s88, 0x4a00
	s_addc_u32 s19, s89, 0
	s_add_u32 s20, s88, 0x4b00
	s_addc_u32 s21, s89, 0
	s_add_u32 s22, s88, 0x4c00
	s_addc_u32 s23, s89, 0
	s_add_u32 s24, s88, 0x4d00
	s_addc_u32 s25, s89, 0
	s_add_u32 s26, s88, 0x4e00
	s_addc_u32 s27, s89, 0
	s_add_u32 s28, s88, 0x4f00
	s_addc_u32 s29, s89, 0
	s_add_u32 s30, s88, 0x5000
	s_addc_u32 s31, s89, 0
	s_add_u32 s34, s88, 0x5100
	s_addc_u32 s35, s89, 0
	s_add_u32 s36, s88, 0x5200
	s_addc_u32 s37, s89, 0
	s_add_u32 s38, s88, 0x5300
	s_addc_u32 s39, s89, 0
	s_mov_b32 s33, 1
	v_mov_b32_e32 v17, 0
	s_branch .LBB0_551

; #define SEAM(k) do { if (IN(k) && IN((k) + 1)) { if ((MK_TAIL_MASK >> (k)) & 1u) moe_pull(F, (k), 0); if ((k) == 9) moe_pull(F, -1, NQ_LATE); if ((k) == 15) moe_pull(F, -1, NQ); xcd_barrier(bar); { int t_ = threadIdx.x; asm volatile("" : "+v"(t_)); F.tid = t_; F.lane = t_ & 63; } } } while (0)
; __global__ void __launch_bounds__(NWAVES * 64, 2) fwd_kernel(Args args) {
;     ...
;     if (IN(10)) { pg8::Gemm g{XN, WSP(const pg8::bf16_t, WS_WIN1), MT, 2 * DM, DM, 0, DM, 0, 0}; pg8::StaticOrder S; S.init(MT, 2 * DM, F.G, (int)blockIdx.x);
;         pg8::EpiBf16 E{WSP(pg8::bf16_t, WS_Z), 2 * DM, 8, 0, 1.0f};
;         pg8::gemm_phase<pg8::EpiBf16, pg8::StaticOrder, true, true>(F.lds, g, S, E); } SEAM(10);
.LBB0_1297:
	v_readlane_b32 s98, v250, 62
	v_and_b32_e32 v2, 15, v0
	v_bfe_u32 v3, v0, 4, 2
	v_lshrrev_b32_e32 v4, 6, v0
	v_lshrrev_b32_e32 v5, 1, v4
	v_and_b32_e32 v6, 1, v4
	s_lshr_b32 s99, s98, 5
	s_lshl_b32 s99, s99, 6
	s_and_b32 s100, s98, 31
	s_lshl_b32 s100, s100, 6
	v_lshl_add_u32 v7, v5, 4, v2
	v_add_u32_e32 v7, s99, v7
	v_lshrrev_b32_e32 v8, 4, v0
	v_lshlrev_b32_e32 v9, 4, v2
	v_add_u32_e32 v10, s99, v8
	v_mul_u32_u24_e32 v10, 0x1000, v10
	v_add_u32_e32 v10, v10, v9
	s_mov_b32 s101, 0x21a00000
	v_add_u32_e32 v10, s101, v10
	v_mov_b32_e32 v11, 0
	v_add_u32_e32 v12, 0x20000, v10
	v_mov_b32_e32 v13, 0
	v_add_u32_e32 v14, s100, v8
	v_mul_u32_u24_e32 v14, 0x1000, v14
	v_add_u32_e32 v14, v14, v9
	s_mov_b32 s101, 0x7800000
	v_add_u32_e32 v14, s101, v14
	v_mov_b32_e32 v15, 0
	v_add_u32_e32 v16, 0x20000, v14
	v_mov_b32_e32 v17, 0
	v_lshl_add_u64 v[10:11], s[88:89], 0, v[10:11]
	v_lshl_add_u64 v[12:13], s[88:89], 0, v[12:13]
	v_lshl_add_u64 v[14:15], s[88:89], 0, v[14:15]
	v_lshl_add_u64 v[16:17], s[88:89], 0, v[16:17]
	v_mul_u32_u24_e32 v18, 272, v8
	v_add_u32_e32 v18, v18, v9
	v_lshl_add_u32 v19, v5, 4, v2
	v_mul_u32_u24_e32 v19, 272, v19
	v_lshl_add_u32 v19, v3, 4, v19
	v_lshl_add_u32 v28, v6, 5, v2
	v_mul_u32_u24_e32 v28, 272, v28
	v_lshl_add_u32 v28, v3, 4, v28
	v_add_u32_e32 v28, 17408, v28
	v_mov_b32_e32 v112, 0x400
	v_mov_b32_e32 v113, 0
	v_mov_b32_e32 v20, 0
	v_mov_b32_e32 v21, 0
	v_mov_b32_e32 v22, 0
	v_mov_b32_e32 v23, 0
	v_mov_b32_e32 v24, 0
	v_mov_b32_e32 v25, 0
	v_mov_b32_e32 v26, 0
	v_mov_b32_e32 v27, 0
	global_load_dwordx4 v[32:35], v[10:11], off offset:0
	global_load_dwordx4 v[36:39], v[12:13], off offset:0
	global_load_dwordx4 v[40:43], v[14:15], off offset:0
	global_load_dwordx4 v[44:47], v[16:17], off offset:0
	global_load_dwordx4 v[48:51], v[10:11], off offset:256
	global_load_dwordx4 v[52:55], v[12:13], off offset:256
	global_load_dwordx4 v[56:59], v[14:15], off offset:256
	global_load_dwordx4 v[60:63], v[16:17], off offset:256
	global_load_dwordx4 v[160:163], v[10:11], off offset:512
	global_load_dwordx4 v[164:167], v[12:13], off offset:512
	global_load_dwordx4 v[168:171], v[14:15], off offset:512
	global_load_dwordx4 v[172:175], v[16:17], off offset:512
	global_load_dwordx4 v[176:179], v[10:11], off offset:768
	global_load_dwordx4 v[180:183], v[12:13], off offset:768
	global_load_dwordx4 v[184:187], v[14:15], off offset:768
	global_load_dwordx4 v[188:191], v[16:17], off offset:768
	s_waitcnt vmcnt(12)
	ds_write_b128 v18, v[32:35] offset:0
	ds_write_b128 v18, v[36:39] offset:8704
	ds_write_b128 v18, v[40:43] offset:17408
	ds_write_b128 v18, v[44:47] offset:26112
	s_waitcnt lgkmcnt(0)
	s_barrier
	s_mov_b32 s101, 4
.Lmg10_kloop:
	global_load_dwordx4 v[32:35], v[10:11], off offset:1024
	global_load_dwordx4 v[36:39], v[12:13], off offset:1024
	global_load_dwordx4 v[40:43], v[14:15], off offset:1024
	global_load_dwordx4 v[44:47], v[16:17], off offset:1024
	s_waitcnt vmcnt(12)
	ds_write_b128 v18, v[48:51] offset:34816
	ds_write_b128 v18, v[52:55] offset:43520
	ds_write_b128 v18, v[56:59] offset:52224
	ds_write_b128 v18, v[60:63] offset:60928
	ds_read_b128 v[64:67], v19 offset:0
	ds_read_b128 v[68:71], v19 offset:64
	ds_read_b128 v[72:75], v19 offset:128
	ds_read_b128 v[76:79], v19 offset:192
	ds_read_b128 v[80:83], v28 offset:0
	ds_read_b128 v[84:87], v28 offset:64
	ds_read_b128 v[88:91], v28 offset:128
	ds_read_b128 v[92:95], v28 offset:192
	ds_read_b128 v[96:99], v28 offset:4352
	ds_read_b128 v[100:103], v28 offset:4416
	ds_read_b128 v[104:107], v28 offset:4480
	ds_read_b128 v[108:111], v28 offset:4544
	s_waitcnt lgkmcnt(0)
	v_mfma_f32_16x16x32_bf16 v[20:23], v[80:83], v[64:67], v[20:23]
	v_mfma_f32_16x16x32_bf16 v[24:27], v[96:99], v[64:67], v[24:27]
	v_mfma_f32_16x16x32_bf16 v[20:23], v[84:87], v[68:71], v[20:23]
	v_mfma_f32_16x16x32_bf16 v[24:27], v[100:103], v[68:71], v[24:27]
	v_mfma_f32_16x16x32_bf16 v[20:23], v[88:91], v[72:75], v[20:23]
	v_mfma_f32_16x16x32_bf16 v[24:27], v[104:107], v[72:75], v[24:27]
	v_mfma_f32_16x16x32_bf16 v[20:23], v[92:95], v[76:79], v[20:23]
	v_mfma_f32_16x16x32_bf16 v[24:27], v[108:111], v[76:79], v[24:27]
	s_waitcnt lgkmcnt(0)
	s_barrier
	global_load_dwordx4 v[48:51], v[10:11], off offset:1280
	global_load_dwordx4 v[52:55], v[12:13], off offset:1280
	global_load_dwordx4 v[56:59], v[14:15], off offset:1280
	global_load_dwordx4 v[60:63], v[16:17], off offset:1280
	s_waitcnt vmcnt(12)
	ds_write_b128 v18, v[160:163] offset:0
	ds_write_b128 v18, v[164:167] offset:8704
	ds_write_b128 v18, v[168:171] offset:17408
	ds_write_b128 v18, v[172:175] offset:26112
	ds_read_b128 v[64:67], v19 offset:34816
	ds_read_b128 v[68:71], v19 offset:34880
	ds_read_b128 v[72:75], v19 offset:34944
	ds_read_b128 v[76:79], v19 offset:35008
	ds_read_b128 v[80:83], v28 offset:34816
	ds_read_b128 v[84:87], v28 offset:34880
	ds_read_b128 v[88:91], v28 offset:34944
	ds_read_b128 v[92:95], v28 offset:35008
	ds_read_b128 v[96:99], v28 offset:39168
	ds_read_b128 v[100:103], v28 offset:39232
	ds_read_b128 v[104:107], v28 offset:39296
	ds_read_b128 v[108:111], v28 offset:39360
	s_waitcnt lgkmcnt(0)
	v_mfma_f32_16x16x32_bf16 v[20:23], v[80:83], v[64:67], v[20:23]
	v_mfma_f32_16x16x32_bf16 v[24:27], v[96:99], v[64:67], v[24:27]
	v_mfma_f32_16x16x32_bf16 v[20:23], v[84:87], v[68:71], v[20:23]
	v_mfma_f32_16x16x32_bf16 v[24:27], v[100:103], v[68:71], v[24:27]
	v_mfma_f32_16x16x32_bf16 v[20:23], v[88:91], v[72:75], v[20:23]
	v_mfma_f32_16x16x32_bf16 v[24:27], v[104:107], v[72:75], v[24:27]
	v_mfma_f32_16x16x32_bf16 v[20:23], v[92:95], v[76:79], v[20:23]
	v_mfma_f32_16x16x32_bf16 v[24:27], v[108:111], v[76:79], v[24:27]
	s_waitcnt lgkmcnt(0)
	s_barrier
; __device__ __forceinline__ unsigned cvt_pk_bf16(float lo, float hi) { unsigned r; asm volatile("v_cvt_pk_bf16_f32 %0, %1, %2" : "=v"(r) : "v"(lo), "v"(hi)); return r; }
;     __device__ __forceinline__ void operator()(const f32x4 (&acc)[2][2][4][2], const Unit& u, int wr, int wc, int fr, int fq) const {
;     ...
;                     u32x4 w; w.x = cvt_pk_bf16(v0[0], v0[1]); w.y = cvt_pk_bf16(v0[2], v0[3]); w.z = cvt_pk_bf16(v1[0], v1[1]); w.w = cvt_pk_bf16(v1[2], v1[3]);
;                     *(u32x4*)(rowp + bj * HALF) = w; } }
; __device__ __forceinline__ void xcd_barrier(const XcdBarrier& b) {
;     asm volatile("s_waitcnt vmcnt(0)" ::: "memory");
;     __syncthreads();
;     if (threadIdx.x == 0) {
;         unsigned* bar = b.bar;
;         __builtin_amdgcn_s_waitcnt(0);
;         unsigned nloc = b.st[0], nx = b.st[1];
;         if (nloc == 0u) { xcd_barrier_complete(bar, b.x, b.total, nloc, nx); b.st[0] = nloc; b.st[1] = nx; }
	global_load_dwordx4 v[160:163], v[10:11], off offset:1536
	global_load_dwordx4 v[164:167], v[12:13], off offset:1536
	global_load_dwordx4 v[168:171], v[14:15], off offset:1536
	global_load_dwordx4 v[172:175], v[16:17], off offset:1536
	s_waitcnt vmcnt(12)
	ds_write_b128 v18, v[176:179] offset:34816
	ds_write_b128 v18, v[180:183] offset:43520
	ds_write_b128 v18, v[184:187] offset:52224
	ds_write_b128 v18, v[188:191] offset:60928
	ds_read_b128 v[64:67], v19 offset:0
	ds_read_b128 v[68:71], v19 offset:64
	ds_read_b128 v[72:75], v19 offset:128
	ds_read_b128 v[76:79], v19 offset:192
	ds_read_b128 v[80:83], v28 offset:0
	ds_read_b128 v[84:87], v28 offset:64
	ds_read_b128 v[88:91], v28 offset:128
	ds_read_b128 v[92:95], v28 offset:192
	ds_read_b128 v[96:99], v28 offset:4352
	ds_read_b128 v[100:103], v28 offset:4416
	ds_read_b128 v[104:107], v28 offset:4480
	ds_read_b128 v[108:111], v28 offset:4544
	s_waitcnt lgkmcnt(0)
	v_mfma_f32_16x16x32_bf16 v[20:23], v[80:83], v[64:67], v[20:23]
	v_mfma_f32_16x16x32_bf16 v[24:27], v[96:99], v[64:67], v[24:27]
	v_mfma_f32_16x16x32_bf16 v[20:23], v[84:87], v[68:71], v[20:23]
	v_mfma_f32_16x16x32_bf16 v[24:27], v[100:103], v[68:71], v[24:27]
	v_mfma_f32_16x16x32_bf16 v[20:23], v[88:91], v[72:75], v[20:23]
	v_mfma_f32_16x16x32_bf16 v[24:27], v[104:107], v[72:75], v[24:27]
	v_mfma_f32_16x16x32_bf16 v[20:23], v[92:95], v[76:79], v[20:23]
	v_mfma_f32_16x16x32_bf16 v[24:27], v[108:111], v[76:79], v[24:27]
	s_waitcnt lgkmcnt(0)
	s_barrier
	global_load_dwordx4 v[176:179], v[10:11], off offset:1792
	global_load_dwordx4 v[180:183], v[12:13], off offset:1792
	global_load_dwordx4 v[184:187], v[14:15], off offset:1792
	global_load_dwordx4 v[188:191], v[16:17], off offset:1792
	s_waitcnt vmcnt(12)
	ds_write_b128 v18, v[32:35] offset:0
	ds_write_b128 v18, v[36:39] offset:8704
	ds_write_b128 v18, v[40:43] offset:17408
	ds_write_b128 v18, v[44:47] offset:26112
	ds_read_b128 v[64:67], v19 offset:34816
	ds_read_b128 v[68:71], v19 offset:34880
	ds_read_b128 v[72:75], v19 offset:34944
	ds_read_b128 v[76:79], v19 offset:35008
	ds_read_b128 v[80:83], v28 offset:34816
	ds_read_b128 v[84:87], v28 offset:34880
	ds_read_b128 v[88:91], v28 offset:34944
	ds_read_b128 v[92:95], v28 offset:35008
	ds_read_b128 v[96:99], v28 offset:39168
	ds_read_b128 v[100:103], v28 offset:39232
	ds_read_b128 v[104:107], v28 offset:39296
	ds_read_b128 v[108:111], v28 offset:39360
	s_waitcnt lgkmcnt(0)
	v_mfma_f32_16x16x32_bf16 v[20:23], v[80:83], v[64:67], v[20:23]
	v_mfma_f32_16x16x32_bf16 v[24:27], v[96:99], v[64:67], v[24:27]
	v_mfma_f32_16x16x32_bf16 v[20:23], v[84:87], v[68:71], v[20:23]
	v_mfma_f32_16x16x32_bf16 v[24:27], v[100:103], v[68:71], v[24:27]
	v_mfma_f32_16x16x32_bf16 v[20:23], v[88:91], v[72:75], v[20:23]
	v_mfma_f32_16x16x32_bf16 v[24:27], v[104:107], v[72:75], v[24:27]
	v_mfma_f32_16x16x32_bf16 v[20:23], v[92:95], v[76:79], v[20:23]
	v_mfma_f32_16x16x32_bf16 v[24:27], v[108:111], v[76:79], v[24:27]
	v_lshl_add_u64 v[10:11], v[10:11], 0, v[112:113]
	v_lshl_add_u64 v[12:13], v[12:13], 0, v[112:113]
	v_lshl_add_u64 v[14:15], v[14:15], 0, v[112:113]
	v_lshl_add_u64 v[16:17], v[16:17], 0, v[112:113]
	s_waitcnt lgkmcnt(0)
	s_barrier
	s_sub_u32 s101, s101, 1
	s_cmp_lg_u32 s101, 0
	s_cbranch_scc1 .Lmg10_kloop
	s_nop 7
	s_nop 7
	v_lshl_add_u32 v116, v6, 5, s100
	v_lshl_add_u32 v116, v3, 2, v116
	v_lshlrev_b32_e32 v116, 1, v116
	v_lshl_add_u32 v116, v7, 13, v116
	s_mov_b32 s101, 0x2e701000
	v_add_u32_e32 v116, s101, v116
	v_mov_b32_e32 v117, 0
	v_lshl_add_u64 v[116:117], s[88:89], 0, v[116:117]
	v_cvt_pk_bf16_f32 v28, v20, v21
	v_cvt_pk_bf16_f32 v29, v22, v23
	v_cvt_pk_bf16_f32 v30, v24, v25
	v_cvt_pk_bf16_f32 v31, v26, v27
	global_store_dwordx2 v[116:117], v[28:29], off
	global_store_dwordx2 v[116:117], v[30:31], off offset:32
	s_cmp_gt_i32 s91, 11
	s_cselect_b64 s[0:1], -1, 0
	s_and_b64 s[2:3], s[4:5], s[0:1]
	s_andn2_b64 vcc, exec, s[2:3]
	s_cbranch_vccnz .LBB0_1351
	s_waitcnt vmcnt(0)
	s_waitcnt vmcnt(0) lgkmcnt(0)
	s_barrier
	s_mov_b64 s[2:3], exec
	v_readlane_b32 s4, v250, 59
	v_readlane_b32 s5, v250, 60
	s_and_b64 s[4:5], s[2:3], s[4:5]
	s_mov_b64 exec, s[4:5]
	s_cbranch_execz .LBB0_1350
	s_add_i32 s4, 0, 0x25020
	v_mov_b32_e32 v1, s4
	s_waitcnt vmcnt(0) expcnt(0) lgkmcnt(0)
	ds_read_b32 v3, v1
	s_add_i32 s4, 0, 0x25024
	v_mov_b32_e32 v1, s4
	ds_read_b32 v1, v1
	s_waitcnt lgkmcnt(1)
	v_cmp_ne_u32_e32 vcc, 0, v3
	s_cbranch_vccnz .LBB0_1314
	s_add_u32 s4, s88, 0x4200
	s_addc_u32 s5, s89, 0
	s_add_u32 s6, s88, 0x4400
	s_addc_u32 s7, s89, 0
	s_add_u32 s8, s88, 0x4500
	s_addc_u32 s9, s89, 0
	s_add_u32 s10, s88, 0x4600
	s_addc_u32 s11, s89, 0
	s_add_u32 s12, s88, 0x4700
	s_addc_u32 s13, s89, 0
	s_add_u32 s14, s88, 0x4800
	s_addc_u32 s15, s89, 0
	s_add_u32 s16, s88, 0x4900
	s_addc_u32 s17, s89, 0
	s_add_u32 s18, s88, 0x4a00
	s_addc_u32 s19, s89, 0
	s_add_u32 s20, s88, 0x4b00
	s_addc_u32 s21, s89, 0
	s_add_u32 s22, s88, 0x4c00
	s_addc_u32 s23, s89, 0
	s_add_u32 s24, s88, 0x4d00
	s_addc_u32 s25, s89, 0
	s_add_u32 s26, s88, 0x4e00
	s_addc_u32 s27, s89, 0
	s_add_u32 s28, s88, 0x4f00
	s_addc_u32 s29, s89, 0
	s_add_u32 s30, s88, 0x5000
	s_addc_u32 s31, s89, 0
	s_add_u32 s34, s88, 0x5100
	s_addc_u32 s35, s89, 0
	s_add_u32 s36, s88, 0x5200
	s_addc_u32 s37, s89, 0
	s_add_u32 s38, s88, 0x5300
	s_addc_u32 s39, s89, 0
	s_mov_b32 s33, 1
	v_mov_b32_e32 v17, 0
	s_branch .LBB0_1302

; #define GAS __attribute__((address_space(1)))
; __device__ __forceinline__ void final_phase(Frame& F) {
;     ...
;         const int e0 = tok_e[2 * row], e1 = tok_e[2 * row + 1]; int o0 = 0, o1 = 0;
; #pragma unroll
;         for (int k = 0; k < 8; ++k) { o0 = (e0 == k) ? off[k] : o0; o1 = (e1 == k) ? off[k] : o1; }
;         const size_t s0 = (size_t)(o0 + tok_rank[2 * row]) * DM, s1 = (size_t)(o1 + tok_rank[2 * row + 1]) * DM; const float w0 = tok_w[2 * row], w1 = tok_w[2 * row + 1];
;         const float* g2 = mod + (size_t)(row >> 13) * MOD_W + 5 * DM;
;         GAS f32x4* xr = (GAS f32x4*)(F.out + (size_t)row * DM) + F.lane;
;         const GAS v2u* hr = (const GAS v2u*)(WSP(const bf16, WS_H) + (size_t)row * DM) + F.lane;
;         f32x4 v[8]; float s = 0.f;
;         const bool tail = __builtin_amdgcn_readfirstlane((int)((s0 >= (size_t)Y2_FULL_TILES * 256 * DM) | (s1 >= (size_t)Y2_FULL_TILES * 256 * DM))) != 0;
.LBB0_2191:
	s_ashr_i32 s17, s16, 31
	s_lshl_b64 s[2:3], s[16:17], 2
	s_add_u32 s0, s38, s2
	s_addc_u32 s1, s39, s3
	global_load_dwordx2 v[0:1], v29, s[0:1]
	s_add_u32 s4, s28, s2
	s_addc_u32 s5, s29, s3
	global_load_dwordx2 v[2:3], v29, s[4:5]
	s_add_i32 s0, s16, 1
	s_ashr_i32 s1, s0, 31
	v_lshlrev_b32_e32 v78, 2, v30
	v_lshlrev_b32_e32 v88, 2, v34
	v_lshlrev_b32_e32 v67, 2, v36
	v_lshlrev_b32_e32 v27, 2, v38
	v_lshlrev_b32_e32 v26, 2, v40
	v_lshlrev_b32_e32 v25, 2, v44
	v_lshlrev_b32_e32 v24, 2, v48
	v_lshlrev_b32_e32 v65, 2, v52
	s_waitcnt vmcnt(0)
	v_readfirstlane_b32 s4, v0
	v_readfirstlane_b32 s5, v1
	s_cmp_eq_u32 s4, 1
	s_cselect_b32 s17, s30, 0
	s_cmp_eq_u32 s5, 1
	s_cselect_b32 s18, s30, 0
	s_cmp_eq_u32 s4, 2
	s_cselect_b32 s17, s31, s17
	s_cmp_eq_u32 s5, 2
	s_cselect_b32 s18, s31, s18
	s_cmp_eq_u32 s4, 3
	s_cselect_b32 s17, s33, s17
	s_cmp_eq_u32 s5, 3
	s_cselect_b32 s18, s33, s18
	s_cmp_eq_u32 s4, 4
	s_cselect_b32 s17, s34, s17
	s_cmp_eq_u32 s5, 4
	s_cselect_b32 s18, s34, s18
	s_cmp_eq_u32 s4, 5
	s_cselect_b32 s17, s35, s17
	s_cmp_eq_u32 s5, 5
	s_cselect_b32 s18, s35, s18
	s_cmp_eq_u32 s4, 6
	s_cselect_b32 s17, s36, s17
	s_cmp_eq_u32 s5, 6
	s_cselect_b32 s18, s36, s18
	s_cmp_eq_u32 s4, 7
	s_cselect_b32 s17, s37, s17
	s_cmp_eq_u32 s5, 7
	s_cselect_b32 s20, s37, s18
	s_lshl_b64 s[18:19], s[0:1], 2
	v_readfirstlane_b32 s0, v2
	s_add_i32 s0, s17, s0
	s_ashr_i32 s1, s0, 31
	s_lshl_b64 s[4:5], s[0:1], 11
	v_readfirstlane_b32 s0, v3
	s_add_i32 s0, s20, s0
	s_ashr_i32 s1, s0, 31
	s_lshl_b64 s[0:1], s[0:1], 11
	s_add_u32 s2, s40, s2
	s_addc_u32 s3, s41, s3
	s_add_u32 s18, s40, s18
	s_addc_u32 s19, s41, s19
	global_load_dword v64, v29, s[2:3]
	global_load_dword v66, v29, s[18:19]
	s_ashr_i32 s2, s6, 13
	s_mul_hi_i32 s3, s2, 0xc000
	s_mul_i32 s2, s2, 0xc000
	s_add_u32 s2, s88, s2
	s_addc_u32 s3, s89, s3
	s_add_u32 s18, s2, 0x12e000
	s_addc_u32 s19, s3, 0
	s_or_b64 s[2:3], s[0:1], s[4:5]
	v_cmp_gt_u64_e32 vcc, s[2:3], v[62:63]
	s_nop 1
	v_cndmask_b32_e64 v0, 0, 1, vcc
	s_nop 0
	v_readfirstlane_b32 s2, v0
	s_bitcmp1_b32 s2, 0
	s_cselect_b64 s[20:21], -1, 0
	s_mov_b64 s[2:3], -1
	s_and_b64 vcc, exec, s[20:21]
	s_cbranch_vccnz .LBB0_2193
	global_load_dwordx2 v[18:19], v[58:59], off
	global_load_dwordx2 v[68:69], v[58:59], off offset:512
	global_load_dwordx2 v[70:71], v[58:59], off offset:1024
	v_lshl_add_u64 v[6:7], s[4:5], 1, v[56:57]
	global_load_dwordx2 v[72:73], v[6:7], off
	v_lshl_add_u64 v[4:5], s[0:1], 1, v[56:57]
	global_load_dwordx2 v[74:75], v[4:5], off
	global_load_dwordx2 v[76:77], v[6:7], off offset:512
	global_load_dwordx2 v[90:91], v[4:5], off offset:512
	global_load_dwordx2 v[92:93], v[6:7], off offset:1024
	global_load_dwordx2 v[94:95], v[4:5], off offset:1024
	global_load_dwordx4 v[8:11], v78, s[18:19]
	global_load_dwordx4 v[12:15], v88, s[18:19]
	global_load_dwordx4 v[80:83], v67, s[18:19]
	global_load_dwordx2 v[96:97], v[6:7], off offset:1536
	global_load_dwordx2 v[98:99], v[4:5], off offset:1536
	global_load_dwordx4 v[84:87], v27, s[18:19]
	global_load_dwordx2 v[100:101], v[58:59], off offset:1536
	global_load_dwordx4 v[0:3], v26, s[18:19]
	global_load_dwordx2 v[16:17], v[58:59], off offset:2048
	global_load_dwordx2 v[102:103], v[6:7], off offset:2048
	global_load_dwordx2 v[20:21], v[6:7], off offset:2560
	global_load_dwordx2 v[104:105], v[4:5], off offset:2048
	global_load_dwordx2 v[22:23], v[4:5], off offset:2560
	s_mov_b64 s[2:3], 0
	s_waitcnt vmcnt(16)
	v_lshlrev_b32_e32 v116, 16, v76
	s_waitcnt vmcnt(15)
	v_lshlrev_b32_e32 v118, 16, v90
	v_and_b32_e32 v119, 0xffff0000, v90
	v_lshlrev_b32_e32 v90, 16, v91
	v_and_b32_e32 v91, 0xffff0000, v91
	v_and_b32_e32 v117, 0xffff0000, v76
	v_lshlrev_b32_e32 v76, 16, v77
	v_and_b32_e32 v77, 0xffff0000, v77
	s_waitcnt vmcnt(13)
	v_lshlrev_b32_e32 v122, 16, v94
	v_and_b32_e32 v123, 0xffff0000, v94
	v_lshlrev_b32_e32 v106, 16, v18
	v_lshlrev_b32_e32 v108, 16, v68
	v_lshlrev_b32_e32 v112, 16, v70
	v_and_b32_e32 v113, 0xffff0000, v70
	v_lshlrev_b32_e32 v114, 16, v71
	v_and_b32_e32 v115, 0xffff0000, v71
	v_lshlrev_b32_e32 v70, 16, v74
	v_and_b32_e32 v71, 0xffff0000, v74
	v_lshlrev_b32_e32 v74, 16, v75
	v_and_b32_e32 v75, 0xffff0000, v75
	v_and_b32_e32 v109, 0xffff0000, v68
	v_lshlrev_b32_e32 v110, 16, v69
	v_and_b32_e32 v111, 0xffff0000, v69
	v_lshlrev_b32_e32 v68, 16, v72
	v_and_b32_e32 v69, 0xffff0000, v72
	v_lshlrev_b32_e32 v72, 16, v73
	v_and_b32_e32 v73, 0xffff0000, v73
	v_pk_mul_f32 v[70:71], v[66:67], v[70:71] op_sel_hi:[0,1]
	v_pk_mul_f32 v[74:75], v[66:67], v[74:75] op_sel_hi:[0,1]
	v_and_b32_e32 v107, 0xffff0000, v18
	v_lshlrev_b32_e32 v18, 16, v19
	v_and_b32_e32 v19, 0xffff0000, v19
	v_pk_mul_f32 v[118:119], v[66:67], v[118:119] op_sel_hi:[0,1]
	v_pk_mul_f32 v[90:91], v[66:67], v[90:91] op_sel_hi:[0,1]
	v_pk_fma_f32 v[68:69], v[64:65], v[68:69], v[70:71] op_sel_hi:[0,1,1]
	v_pk_fma_f32 v[72:73], v[64:65], v[72:73], v[74:75] op_sel_hi:[0,1,1]
	v_lshlrev_b32_e32 v120, 16, v92
	v_and_b32_e32 v121, 0xffff0000, v92
	v_lshlrev_b32_e32 v94, 16, v95
	v_and_b32_e32 v95, 0xffff0000, v95
	v_pk_mul_f32 v[122:123], v[66:67], v[122:123] op_sel_hi:[0,1]
	v_pk_fma_f32 v[74:75], v[64:65], v[116:117], v[118:119] op_sel_hi:[0,1,1]
	v_pk_fma_f32 v[76:77], v[64:65], v[76:77], v[90:91] op_sel_hi:[0,1,1]
	s_waitcnt vmcnt(12)
	v_pk_fma_f32 v[70:71], v[8:9], v[68:69], v[106:107]
	v_pk_fma_f32 v[68:69], v[10:11], v[72:73], v[18:19]
	v_lshlrev_b32_e32 v92, 16, v93
	v_and_b32_e32 v93, 0xffff0000, v93
	v_pk_mul_f32 v[94:95], v[66:67], v[94:95] op_sel_hi:[0,1]
	v_pk_fma_f32 v[90:91], v[64:65], v[120:121], v[122:123] op_sel_hi:[0,1,1]
	s_waitcnt vmcnt(11)
; #define GAS __attribute__((address_space(1)))
; __device__ __forceinline__ void final_phase(Frame& F) {
;     ...
;         if (!tail) {
; #pragma unroll
;             for (int j = 0; j < 8; ++j) { const int col = 4 * (F.lane + 64 * j);
;                 const v2u ya = *(const GAS v2u*)(Y2 + s0 + col), yb = *(const GAS v2u*)(Y2 + s1 + col); const f32x4 gg = *(const GAS f32x4*)(g2 + col);
;                 f32x4 mo; mo.x = w0 * bflo(ya.x) + w1 * bflo(yb.x); mo.y = w0 * bfhi(ya.x) + w1 * bfhi(yb.x); mo.z = w0 * bflo(ya.y) + w1 * bflo(yb.y); mo.w = w0 * bfhi(ya.y) + w1 * bfhi(yb.y);
;                 { const v2u hw = hr[64 * j]; f32x4 hv; hv.x = bflo(hw.x); hv.y = bfhi(hw.x); hv.z = bflo(hw.y); hv.w = bfhi(hw.y); v[j] = hv + gg * mo; } s += (v[j].x * v[j].x + v[j].y * v[j].y) + (v[j].z * v[j].z + v[j].w * v[j].w); }
	v_pk_fma_f32 v[74:75], v[12:13], v[74:75], v[108:109]
	v_pk_fma_f32 v[72:73], v[14:15], v[76:77], v[110:111]
	v_pk_mul_f32 v[12:13], v[68:69], v[68:69]
	v_pk_mul_f32 v[14:15], v[70:71], v[70:71]
	v_pk_fma_f32 v[92:93], v[64:65], v[92:93], v[94:95] op_sel_hi:[0,1,1]
	s_waitcnt vmcnt(10)
	v_pk_fma_f32 v[8:9], v[80:81], v[90:91], v[112:113]
	v_pk_mul_f32 v[18:19], v[72:73], v[72:73]
	v_pk_mul_f32 v[76:77], v[74:75], v[74:75]
	v_pk_mov_b32 v[80:81], v[14:15], v[12:13] op_sel:[1,0]
	v_mov_b32_e32 v15, v13
	global_load_dwordx2 v[94:95], v[58:59], off offset:2560
	v_pk_fma_f32 v[10:11], v[82:83], v[92:93], v[114:115]
	v_pk_mov_b32 v[12:13], v[76:77], v[18:19] op_sel:[1,0]
	v_mov_b32_e32 v77, v19
	v_pk_add_f32 v[18:19], v[80:81], v[14:15]
	s_waitcnt vmcnt(9)
	v_lshlrev_b32_e32 v14, 16, v98
	global_load_dwordx4 v[80:83], v25, s[18:19]
	v_and_b32_e32 v15, 0xffff0000, v98
	global_load_dwordx2 v[108:109], v[4:5], off offset:3072
	global_load_dwordx2 v[106:107], v[6:7], off offset:3072
	v_pk_add_f32 v[76:77], v[12:13], v[76:77]
	v_lshlrev_b32_e32 v12, 16, v96
	v_and_b32_e32 v13, 0xffff0000, v96
	v_pk_mul_f32 v[14:15], v[66:67], v[14:15] op_sel_hi:[0,1]
	v_lshlrev_b32_e32 v90, 16, v99
	v_and_b32_e32 v91, 0xffff0000, v99
	v_pk_fma_f32 v[12:13], v[64:65], v[12:13], v[14:15] op_sel_hi:[0,1,1]
	v_lshlrev_b32_e32 v14, 16, v97
	v_and_b32_e32 v15, 0xffff0000, v97
	v_pk_mul_f32 v[90:91], v[66:67], v[90:91] op_sel_hi:[0,1]
	v_pk_fma_f32 v[14:15], v[64:65], v[14:15], v[90:91] op_sel_hi:[0,1,1]
	global_load_dwordx2 v[98:99], v[58:59], off offset:3072
	s_waitcnt vmcnt(11)
	v_lshlrev_b32_e32 v90, 16, v101
	v_and_b32_e32 v91, 0xffff0000, v101
	v_lshlrev_b32_e32 v96, 16, v100
	v_and_b32_e32 v97, 0xffff0000, v100
	v_pk_fma_f32 v[14:15], v[86:87], v[14:15], v[90:91]
	global_load_dwordx4 v[90:93], v24, s[18:19]
	v_pk_fma_f32 v[12:13], v[84:85], v[12:13], v[96:97]
	v_pk_add_f32 v[18:19], v[18:19], v[18:19] op_sel:[0,1] op_sel_hi:[1,0]
	v_mul_f32_e32 v28, v12, v12
	v_mul_f32_e32 v79, v13, v13
	v_pk_add_f32 v[76:77], v[76:77], v[76:77] op_sel:[0,1] op_sel_hi:[1,0]
	v_mov_b32_e32 v19, v28
	v_mov_b32_e32 v77, v79
	v_mul_f32_e32 v28, v9, v9
	v_mul_f32_e32 v84, v14, v14
	v_pk_add_f32 v[18:19], v[18:19], v[76:77]
	v_pk_fma_f32 v[76:77], v[8:9], v[8:9], v[28:29] op_sel_hi:[1,1,0]
	v_mul_f32_e32 v28, v11, v11
	v_mul_f32_e32 v86, v15, v15
	v_mov_b32_e32 v77, v84
	v_pk_fma_f32 v[84:85], v[10:11], v[10:11], v[28:29] op_sel_hi:[1,1,0]
	global_load_dwordx2 v[96:97], v[58:59], off offset:3584
	v_mov_b32_e32 v85, v86
	v_pk_add_f32 v[76:77], v[76:77], v[84:85]
	global_load_dwordx2 v[84:85], v[6:7], off offset:3584
	global_load_dwordx2 v[86:87], v[4:5], off offset:3584
	s_waitcnt vmcnt(10)
	v_lshlrev_b32_e32 v4, 16, v104
	v_and_b32_e32 v5, 0xffff0000, v104
	v_lshlrev_b32_e32 v6, 16, v102
	v_and_b32_e32 v7, 0xffff0000, v102
	v_pk_mul_f32 v[4:5], v[66:67], v[4:5] op_sel_hi:[0,1]
	v_pk_add_f32 v[76:77], v[18:19], v[76:77]
	v_pk_fma_f32 v[18:19], v[64:65], v[6:7], v[4:5] op_sel_hi:[0,1,1]
	v_lshlrev_b32_e32 v6, 16, v105
	v_and_b32_e32 v7, 0xffff0000, v105
	v_lshlrev_b32_e32 v4, 16, v103
	v_and_b32_e32 v5, 0xffff0000, v103
	v_pk_mul_f32 v[6:7], v[66:67], v[6:7] op_sel_hi:[0,1]
	v_pk_fma_f32 v[100:101], v[64:65], v[4:5], v[6:7] op_sel_hi:[0,1,1]
	global_load_dwordx4 v[4:7], v65, s[18:19]
	v_lshlrev_b32_e32 v102, 16, v16
	v_and_b32_e32 v103, 0xffff0000, v16
	v_lshlrev_b32_e32 v104, 16, v17
	v_and_b32_e32 v105, 0xffff0000, v17
	v_pk_fma_f32 v[16:17], v[0:1], v[18:19], v[102:103]
	v_pk_fma_f32 v[18:19], v[2:3], v[100:101], v[104:105]
	v_pk_mul_f32 v[2:3], v[16:17], v[16:17]
	v_pk_mul_f32 v[0:1], v[18:19], v[18:19]
	v_pk_add_f32 v[76:77], v[76:77], v[76:77] op_sel:[0,1] op_sel_hi:[1,0]
	v_pk_mov_b32 v[100:101], v[2:3], v[0:1] op_sel:[1,0]
	v_mov_b32_e32 v3, v1
	v_pk_add_f32 v[100:101], v[100:101], v[2:3]
	s_waitcnt vmcnt(10)
	v_lshlrev_b32_e32 v2, 16, v22
	v_and_b32_e32 v3, 0xffff0000, v22
	v_lshlrev_b32_e32 v0, 16, v20
	v_and_b32_e32 v1, 0xffff0000, v20
	v_pk_mul_f32 v[2:3], v[66:67], v[2:3] op_sel_hi:[0,1]
	v_pk_fma_f32 v[0:1], v[64:65], v[0:1], v[2:3] op_sel_hi:[0,1,1]
	v_lshlrev_b32_e32 v2, 16, v21
	v_and_b32_e32 v3, 0xffff0000, v21
	v_lshlrev_b32_e32 v20, 16, v23
	v_and_b32_e32 v21, 0xffff0000, v23
	v_pk_mul_f32 v[20:21], v[66:67], v[20:21] op_sel_hi:[0,1]
	v_pk_fma_f32 v[2:3], v[64:65], v[2:3], v[20:21] op_sel_hi:[0,1,1]
	s_waitcnt vmcnt(9)
	v_lshlrev_b32_e32 v22, 16, v95
	v_and_b32_e32 v23, 0xffff0000, v95
	v_lshlrev_b32_e32 v20, 16, v94
	v_and_b32_e32 v21, 0xffff0000, v94
	s_waitcnt vmcnt(8)
	v_pk_fma_f32 v[22:23], v[82:83], v[2:3], v[22:23]
	s_waitcnt vmcnt(7)
	v_lshlrev_b32_e32 v2, 16, v108
	v_and_b32_e32 v3, 0xffff0000, v108
	v_pk_fma_f32 v[20:21], v[80:81], v[0:1], v[20:21]
	s_waitcnt vmcnt(6)
	v_lshlrev_b32_e32 v0, 16, v106
	v_and_b32_e32 v1, 0xffff0000, v106
	v_pk_mul_f32 v[2:3], v[66:67], v[2:3] op_sel_hi:[0,1]
	v_lshlrev_b32_e32 v80, 16, v109
	v_and_b32_e32 v81, 0xffff0000, v109
	v_pk_fma_f32 v[0:1], v[64:65], v[0:1], v[2:3] op_sel_hi:[0,1,1]
	v_lshlrev_b32_e32 v2, 16, v107
	v_and_b32_e32 v3, 0xffff0000, v107
	v_pk_mul_f32 v[80:81], v[66:67], v[80:81] op_sel_hi:[0,1]
	v_pk_fma_f32 v[2:3], v[64:65], v[2:3], v[80:81] op_sel_hi:[0,1,1]
	s_waitcnt vmcnt(5)
	v_lshlrev_b32_e32 v80, 16, v98
	v_and_b32_e32 v81, 0xffff0000, v98
	v_lshlrev_b32_e32 v82, 16, v99
	s_waitcnt vmcnt(4)
	v_pk_fma_f32 v[0:1], v[90:91], v[0:1], v[80:81]
	v_and_b32_e32 v83, 0xffff0000, v99
	v_mul_f32_e32 v28, v0, v0
	v_mul_f32_e32 v79, v1, v1
	v_pk_add_f32 v[80:81], v[100:101], v[100:101] op_sel:[0,1] op_sel_hi:[1,0]
	v_pk_fma_f32 v[2:3], v[92:93], v[2:3], v[82:83]
	v_mov_b32_e32 v77, v28
	v_mov_b32_e32 v81, v79
	v_mul_f32_e32 v28, v21, v21
	v_mul_f32_e32 v82, v2, v2
	v_pk_add_f32 v[76:77], v[76:77], v[80:81]
	v_pk_fma_f32 v[80:81], v[20:21], v[20:21], v[28:29] op_sel_hi:[1,1,0]
	v_mul_f32_e32 v28, v23, v23
	v_mul_f32_e32 v89, v3, v3
	v_mov_b32_e32 v81, v82
	v_pk_fma_f32 v[82:83], v[22:23], v[22:23], v[28:29] op_sel_hi:[1,1,0]
	s_nop 0
	v_mov_b32_e32 v83, v89
	v_pk_add_f32 v[80:81], v[80:81], v[82:83]
	s_waitcnt vmcnt(1)
	v_lshlrev_b32_e32 v82, 16, v87
	v_pk_add_f32 v[76:77], v[76:77], v[80:81]
	v_lshlrev_b32_e32 v80, 16, v86
	v_and_b32_e32 v81, 0xffff0000, v86
	v_add_f32_e32 v28, v76, v77
	v_lshlrev_b32_e32 v76, 16, v84
	v_and_b32_e32 v77, 0xffff0000, v84
	v_pk_mul_f32 v[80:81], v[66:67], v[80:81] op_sel_hi:[0,1]
	v_and_b32_e32 v83, 0xffff0000, v87
	v_pk_fma_f32 v[76:77], v[64:65], v[76:77], v[80:81] op_sel_hi:[0,1,1]
	v_lshlrev_b32_e32 v80, 16, v85
	v_and_b32_e32 v81, 0xffff0000, v85
	v_pk_mul_f32 v[82:83], v[66:67], v[82:83] op_sel_hi:[0,1]
	v_pk_fma_f32 v[80:81], v[64:65], v[80:81], v[82:83] op_sel_hi:[0,1,1]
	v_lshlrev_b32_e32 v82, 16, v96
	v_and_b32_e32 v83, 0xffff0000, v96
	v_lshlrev_b32_e32 v84, 16, v97
	v_and_b32_e32 v85, 0xffff0000, v97
	s_waitcnt vmcnt(0)
	v_pk_fma_f32 v[6:7], v[6:7], v[80:81], v[84:85]
	v_pk_fma_f32 v[4:5], v[4:5], v[76:77], v[82:83]
